# DATT: one static s_setprio 1 for waves 4..7 at phase entry (reset at phase exit)
# speedup vs baseline: 1.0053x; 1.0005x over previous
; __device__ __forceinline__ void datt_stream(LAS unsigned char* lds, const DattRun& c, const float C, const int wv) {
;     const int NP = c.np, NS = NP + 2; constexpr int HALFWIN = 64;
;     const int tid = otid(wv), wid = __builtin_amdgcn_readfirstlane(tid >> 6), lane = tid & 63, r32 = lane & 31, hi = lane >> 5, par = wid & 1, pa0 = wid >> 1;
;     LAS unsigned char* V_lds = lds; LAS unsigned char* K_lds = lds + 2 * SHM_T; LAS unsigned char* stg = lds + 65536 + wid * 8192;
;     LAS float* wsf = (LAS float*)(lds + 132096) + wid * 64; LAS float* li_l = wsf; LAS float* al_l = wsf + 32;
;     auto rowoff = [&](int idx) __attribute__((always_inline)) { return (size_t)(idx * c.dil + c.r) * ODD_IN + c.g * 3072 + c.h * 128; };
;     const bool edge = (c.a0 == 0) || (64 * (c.a0 + NP) >= c.L);
;     const int sr = tid >> 4, sc = (tid & 15) * 8;
;     const int vst0 = v_st(sr, sc), vst1 = v_st(32 + sr, sc), kst0 = ATT_KSWZ(sr, sc * 2), kst1 = ATT_KSWZ(32 + sr, sc * 2);
;     const int vb0 = (int)(unsigned)(uintptr_t)V_lds + v_rd_base(lane);
;     u32x2 ksA0, ksA1, vsA0, vsA1, ksB0, ksB1, vsB0, vsB1;
;     const unsigned char* zb = c.z + c.g * 3072 + c.h * 128;
;     auto roff = [&](int idx) __attribute__((always_inline)) { return (unsigned)(idx * c.dil + c.r) * (unsigned)ODD_IN; };
; template <int PH, bool PRB = false>
; __device__ __forceinline__ void run_phase(int layer, LAS unsigned char* lds, const int wv_) {
;     ...
;     if constexpr (PH == PH_DATT) {
;         float* lse = (float*)(ws + WS_MISC + MISC_LSE);
;         LAS float* tb = (LAS float*)(lds + 132096 + 4096);
;         for (int it = bid; it < 512; it += G) {
;             const bool dbl = it < 256; const int g = dbl ? (it >> 7) : 2, cc = dbl ? (it & 127) : (it - 256), hh = cc & 7, rest = cc >> 3;
;             const int dil = g == 0 ? 1 : (g == 1 ? 4 : 16), r = rest % dil, chunk = rest / dil;
;             { const int t2 = otid(wv); if (t2 < 256) { const int d = t2 - 128; tb[t2] = (d >= -64 && d <= 64) ? bto[(g * 8 + hh) * 129 + d + 64] * 1.4426950408889634f : -__builtin_inff(); } }
;             att::DattRun R{ws + WS_Z, (bf16*)(ws + WS_Z + Z_OB), PRB ? (float*)(ws + WS_H + 26 * MiB) : lse, tb, g, hh, dil, r, chunk * (dbl ? 16 : 8), S / dil, PRB ? y : nullptr, dbl ? 16 : 8};
;             att::datt_stream(lds, R, 0.08838834764831845f * 1.4426950408889634f, wv);
.LBB0_403:
	s_bitcmp1_b32 s80, 0
	s_cselect_b64 s[2:3], -1, 0
	s_mov_b64 s[0:1], -1
	s_and_b64 vcc, exec, s[2:3]
	v_writelane_b32 v255, s80, 1
	s_waitcnt lgkmcnt(0)
	s_barrier
	s_cbranch_vccz .LBB0_636
	s_mov_b64 s[0:1], 0
	s_mov_b32 s100, 0
	s_mov_b32 s101, 0
	v_readlane_b32 s98, v254, 8
	s_cmp_ge_u32 s98, 4
	s_cbranch_scc0 .Lprio_skip
	s_setprio 1
.Lprio_skip:
	s_mov_b32 s2, s80
	v_mbcnt_lo_u32_b32 v0, -1, 0
	v_mbcnt_hi_u32_b32 v0, -1, v0
	v_readlane_b32 s50, v254, 0
	v_add_u32_e32 v0, s93, v0
	s_cmpk_gt_i32 s50, 0x1ff
	s_cbranch_scc1 .LBB0_524
	v_readlane_b32 s2, v254, 1
	v_readlane_b32 s3, v254, 2
	s_add_u32 s0, s2, s0
	s_addc_u32 s1, s3, s1
	s_load_dwordx2 s[0:1], s[0:1], 0xe0
	s_waitcnt lgkmcnt(0)
	s_add_u32 s2, s0, 0x8100000
	v_writelane_b32 v255, s2, 2
	s_addc_u32 s2, s1, 0
	v_writelane_b32 v255, s2, 3
	s_add_u32 s2, s0, 0x21c00000
	v_writelane_b32 v255, s2, 4
	s_addc_u32 s2, s1, 0
	v_writelane_b32 v255, s2, 5
	s_add_u32 s2, s0, 0x11100000
	v_writelane_b32 v255, s2, 6
	v_writelane_b32 v255, s0, 7
	s_nop 1
	v_writelane_b32 v255, s1, 8
	s_addc_u32 s0, s1, 0
	v_writelane_b32 v255, s0, 9
	s_branch .LBB0_407

; __device__ __forceinline__ int lane_id() { int l; asm volatile("v_mbcnt_lo_u32_b32 %0, -1, 0\n\tv_mbcnt_hi_u32_b32 %0, -1, %0" : "=v"(l)); return l; }
; __device__ __forceinline__ void xcd_barrier(const XcdBarrier& b, const int wv) {
;     asm volatile("s_waitcnt vmcnt(0)" ::: "memory");
;     __syncthreads();
;     if (wv == 0 && lane_id() == 0) {
;         unsigned long long bzo = 0ull; unsigned bx = b.x; asm volatile("" : "+s"(bzo), "+s"(bx)); unsigned* bar = b.bar + bzo;
;         __builtin_amdgcn_s_waitcnt(0);
;         unsigned nloc = b.st[0], nx = b.st[1];
;         if (nloc == 0u) { xcd_barrier_complete(bar, bx, nloc, nx); b.st[0] = nloc; b.st[1] = nx; }
; template <int PH, bool PRB = false>
; __device__ __forceinline__ void run_phase(int layer, LAS unsigned char* lds, const int wv_) {
;     ...
;             att::datt_stream(lds, R, 0.08838834764831845f * 1.4426950408889634f, wv);
;         }
.LBB0_524:
	s_setprio 0
	s_waitcnt vmcnt(0)
	s_and_b64 vcc, exec, s[78:79]
	s_barrier
	s_cbranch_vccnz .LBB0_576
	v_mbcnt_lo_u32_b32 v0, -1, 0
	v_mbcnt_hi_u32_b32 v0, -1, v0
	s_nop 0
	v_cmp_eq_u32_e32 vcc, 0, v0
	s_and_saveexec_b64 s[0:1], vcc
	s_cbranch_execz .LBB0_575
	v_readlane_b32 s18, v254, 5
	s_mov_b64 s[2:3], 0
	v_readlane_b32 s4, v254, 23
	s_lshl_b64 s[2:3], s[2:3], 2
	s_waitcnt vmcnt(0) expcnt(0) lgkmcnt(0)
	v_mov_b32_e32 v0, s4
	v_readlane_b32 s4, v254, 3
	ds_read_b32 v2, v0
	s_add_u32 s2, s4, s2
	v_readlane_b32 s4, v254, 24
	v_readlane_b32 s5, v254, 4
	s_addc_u32 s3, s5, s3
	v_mov_b32_e32 v0, s4
	ds_read_b32 v0, v0
	s_waitcnt lgkmcnt(1)
	v_cmp_ne_u32_e32 vcc, 0, v2
	s_cbranch_vccnz .LBB0_541
	s_add_u32 s4, s2, 0x1000
	s_addc_u32 s5, s3, 0
	s_add_u32 s6, s2, 0x1100
	s_addc_u32 s7, s3, 0
	s_add_u32 s8, s2, 0x1200
	s_addc_u32 s9, s3, 0
	s_add_u32 s10, s2, 0x1300
	s_addc_u32 s11, s3, 0
	s_mov_b32 s19, 1
	s_branch .LBB0_529
